# LN+router pass 1: removed four compiler vmcnt(0) drains in the next-row prefetch of the bf16-input path (they guarded registers only the f32-input path loads); the eight prefetch loads now issue back
# speedup vs baseline: 1.0189x; 1.0052x over previous
.LBB0_920:
	v_mov_b64_e32 v[16:17], v[120:121]
	s_andn2_b64 vcc, exec, s[8:9]
	v_mov_b64_e32 v[18:19], v[122:123]
	s_cbranch_vccnz .LBB0_922
	v_lshl_add_u64 v[8:9], v[152:153], 1, s[30:31]
	global_load_dwordx4 v[16:19], v[8:9], off nt
	v_mov_b64_e32 v[12:13], v[100:101]
	v_mov_b64_e32 v[8:9], v[116:117]
	v_mov_b64_e32 v[14:15], v[102:103]
	v_mov_b64_e32 v[10:11], v[118:119]

.LBB0_924:
	v_mov_b64_e32 v[32:33], v[124:125]
	s_andn2_b64 vcc, exec, s[8:9]
	v_mov_b64_e32 v[34:35], v[126:127]
	s_cbranch_vccnz .LBB0_926
	v_lshl_add_u64 v[24:25], v[36:37], 1, s[30:31]
	global_load_dwordx4 v[32:35], v[24:25], off nt
	v_mov_b64_e32 v[28:29], v[96:97]
	v_mov_b64_e32 v[24:25], v[112:113]
	v_mov_b64_e32 v[30:31], v[98:99]
	v_mov_b64_e32 v[26:27], v[114:115]

.LBB0_928:
	v_mov_b64_e32 v[48:49], v[128:129]
	s_andn2_b64 vcc, exec, s[8:9]
	v_mov_b64_e32 v[50:51], v[130:131]
	s_cbranch_vccnz .LBB0_930
	v_lshl_add_u64 v[40:41], v[52:53], 1, s[30:31]
	global_load_dwordx4 v[48:51], v[40:41], off nt
	v_mov_b64_e32 v[44:45], v[92:93]
	v_mov_b64_e32 v[40:41], v[108:109]
	v_mov_b64_e32 v[46:47], v[94:95]
	v_mov_b64_e32 v[42:43], v[110:111]

.LBB0_932:
	v_mov_b64_e32 v[64:65], v[132:133]
	s_andn2_b64 vcc, exec, s[8:9]
	v_mov_b64_e32 v[66:67], v[134:135]
	s_cbranch_vccnz .LBB0_916
	v_lshl_add_u64 v[56:57], v[152:153], 1, s[30:31]
	global_load_dwordx4 v[64:67], v[56:57], off nt
	v_mov_b64_e32 v[56:57], v[104:105]
	v_mov_b64_e32 v[60:61], v[88:89]
	v_mov_b64_e32 v[58:59], v[106:107]
	v_mov_b64_e32 v[62:63], v[90:91]
	s_branch .LBB0_916
